# v18 = v16 + half of the workgroups run phase 5 in the opposite order (attention first, then RWKV scan) to overlap attention with the other half's HBM-bound scan
# baseline (speedup 1.0000x reference)
; #define RUN(grp, ...) do { for (int rep_ = 0; rep_ < ((PROBE == (grp)) ? 2 : 1); ++rep_) { __VA_ARGS__ } } while (0)
; __global__ void __launch_bounds__(NTHR, 2) k_all(Params p) {
;     ...
;     RUN(3, ph_rwscan(p, lds, wg, nwg, ct_split); ph_naattn(p, lds, wg, nwg);); xcd_barrier(bar);
.LBB0_606:
	s_or_b64 exec, exec, s[0:1]
	v_writelane_b32 v249, s6, 0
	v_writelane_b32 v249, s12, 1
	v_writelane_b32 v249, s14, 2
	v_writelane_b32 v249, s15, 3
	v_writelane_b32 v249, s18, 4
	v_writelane_b32 v249, s19, 5
	v_writelane_b32 v249, s20, 6
	v_writelane_b32 v249, s21, 7
	v_writelane_b32 v249, s22, 8
	v_writelane_b32 v249, s23, 9
	v_writelane_b32 v249, s24, 10
	v_writelane_b32 v249, s25, 11
	v_writelane_b32 v249, s34, 12
	v_writelane_b32 v249, s35, 13
	v_writelane_b32 v249, s39, 14
	v_writelane_b32 v249, s46, 15
	v_writelane_b32 v249, s47, 16
	v_writelane_b32 v249, s48, 17
	v_writelane_b32 v249, s49, 18
	v_writelane_b32 v249, s74, 19
	v_writelane_b32 v249, s75, 20
	v_writelane_b32 v249, s76, 21
	v_writelane_b32 v249, s77, 22
	v_writelane_b32 v249, s88, 23
	v_writelane_b32 v249, s90, 24
	v_writelane_b32 v249, s91, 25
	v_writelane_b32 v249, s92, 26
	v_writelane_b32 v249, s93, 27
	v_writelane_b32 v249, s96, 28
	v_writelane_b32 v249, s97, 29
	v_mov_b32_e32 v250, v5
	v_mov_b32_e32 v251, v245
	v_mov_b32_e32 v252, v248
	s_bfe_u32 s98, s90, 0x10003
	s_mov_b32 s99, 0
	v_writelane_b32 v249, s98, 60
	v_writelane_b32 v249, s99, 61
	v_writelane_b32 v249, s98, 62
; __device__ __forceinline__ int ptid() { int t = threadIdx.x; asm volatile("" : "+v"(t)); return t; }
; #define CT_LOADNT(T_) do { const int tt_ = (T_) < CT_TOTAL ? (T_) : CT_TOTAL - 1; const ConvTile ct_ = conv_tile_desc(cttab, tt_); const int ckq_ = lane >> 4, ccol_ = ((lane & 15) * 4 < ct_.nvalid) ? (lane & 15) * 4 : 0; CT_FORQ(CT_LOAD1NT) } while (0)
; __device__ __forceinline__ void ph_rwscan(const Params& p, float* lds, int wg, int nwg, int ct_begin) {
;     const int tid = ptid(), wave = __builtin_amdgcn_readfirstlane(tid >> 6), lane = tid & 63;
;     const bool loader = wave >= 4;
;     for (int unit = wg; unit < 256; unit += nwg) {
;         const int rg = (unit >> 3) & 3, grp_ = (unit >> 5) * 8 + (unit & 7);
;         const int b = grp_ >> 5, h = (grp_ >> 1) & 15, dir = grp_ & 1;
;         const int lt = tid & 255;
;         const float* const aW = dir ? p.W[1] : p.W[0]; const bf16_t* const aN = dir ? p.NB[1] : p.NB[0]; const bf16_t* const aD = dir ? p.KD[1] : p.KD[0];
;         const int st0 = lt >> 4, st1 = 16 + (lt >> 4), c4l = lt & 15, sth = lt >> 3, c8l = lt & 7, qv = lt < 128 ? lt : 127, stv = qv >> 2, cvl = qv & 3;
;         float4 rAW0, rAW1, rAV, rBW0, rBW1, rBV; uint4 rAK, rAN, rAD, rAR, rBK, rBN, rBD, rBR;
;     ...
;         float* buf0 = lds; float* buf1 = lds + RW_TB * RW_STEPF;
;         float4 cv0, cv1, cv2, cv3, cv4, cv5, cv6, cv7;
;         const unsigned long long* cttab = (const unsigned long long*)((const char*)lds + CTTAB_OFF);
;         const int cgw = wg * 4 + (wave - 4), cnw = nwg * 4;
;         char* const ctlds = (char*)lds + 2 * RW_TB * RW_STEPF * 4 + (wave - 4) * CT_LDS_BYTES;
;         if (loader) { RW_LOAD_BLOCK(0, A); RW_WRITE_BLOCK(buf0, A); RW_LOAD_BLOCK(1, A); RW_LOAD_BLOCK(2, B); CT_LOADNT(ct_begin + cgw); }
;         __syncthreads();
;         f2v Sa = {0.f, 0.f}, Sb = {0.f, 0.f};
;         float* const Yd = dir ? p.Y[1] : p.Y[0];
;         const int seg = lane & 15, vrl = wave * 4 + (lane >> 4);
.Lswap_top:
	v_readlane_b32 s2, v248, 43
	s_waitcnt lgkmcnt(0)
	v_mov_b32_e32 v2, v0
	v_readlane_b32 s3, v248, 44
	s_barrier
	s_and_b64 vcc, exec, s[2:3]
	v_readfirstlane_b32 s0, v2
	v_readlane_b32 s98, v249, 60
	s_nop 3
	s_cmp_lg_u32 s98, 0
	s_cselect_b64 vcc, 0, vcc
	s_nop 0
	s_cbranch_vccz .LBB0_751
	v_writelane_b32 v248, s34, 55
	s_lshl_b32 s80, s96, 2
	s_ashr_i32 s2, s0, 6
	v_writelane_b32 v248, s35, 56
	v_writelane_b32 v248, s92, 57
	s_cmp_lt_i32 s2, 4
	s_cselect_b64 s[0:1], -1, 0
	v_writelane_b32 v248, s93, 58
	s_lshl_b32 s3, s90, 2
	v_readlane_b32 s4, v248, 37
	s_add_i32 s3, s4, s3
	s_add_i32 s3, s3, s2
	s_add_i32 s5, s3, 0x63fc
	s_min_i32 s3, s5, 0x324ff
	s_cmpk_gt_i32 s5, 0x19ff
	s_cselect_b64 s[6:7], -1, 0
	v_writelane_b32 v248, s6, 53
	s_cmpk_gt_i32 s5, 0x21ff
	v_and_b32_e32 v137, 15, v2
	v_writelane_b32 v248, s7, 54
	s_cselect_b64 s[6:7], -1, 0
	v_writelane_b32 v248, s6, 47
	s_cmpk_gt_i32 s5, 0x4dff
	v_bfe_u32 v131, v2, 4, 4
	v_writelane_b32 v248, s7, 48
	s_cselect_b64 s[6:7], -1, 0
	v_writelane_b32 v248, s6, 59
	s_cmpk_gt_i32 s5, 0x63ff
	s_movk_i32 s4, 0x7f
	v_writelane_b32 v248, s7, 60
	s_cselect_b64 s[6:7], -1, 0
	v_writelane_b32 v248, s6, 61
	s_cmpk_gt_i32 s5, 0x7cff
	v_mul_u32_u24_e32 v6, 5, v137
	v_writelane_b32 v248, s7, 62
	s_cselect_b64 s[6:7], -1, 0
	v_writelane_b32 v248, s6, 63
	s_cmp_gt_i32 s5, 0x84ff
	v_writelane_b32 v248, s5, 45
	v_writelane_b32 v245, s7, 0
	s_cselect_b64 s[6:7], -1, 0
	s_cmp_gt_i32 s5, 0x244ff
	s_cselect_b64 s[14:15], -1, 0
	s_add_i32 s8, s3, 0xffff7b00
	s_lshr_b32 s9, s8, 11
	s_mul_hi_u32 s9, s9, 0x24924925
	s_mul_i32 s10, s9, 0x3800
	s_sub_i32 s8, s8, s10
	s_bfe_u32 s10, s8, 0x100005
	s_mulk_i32 s10, 0x2493
	s_lshr_b32 s10, s10, 16
	v_writelane_b32 v245, s6, 1
	s_mul_i32 s11, s10, 0xe0
	s_sub_i32 s8, s8, s11
	v_writelane_b32 v245, s7, 2
	s_add_i32 s11, s3, 0xffff8300
	s_and_b32 s12, s3, 31
	v_writelane_b32 v245, s12, 3
	s_lshr_b32 s11, s11, 5
	v_writelane_b32 v245, s11, 5
	s_add_i32 s11, s3, 0x9c00
	s_bfe_u32 s12, s11, 0xe0002
	s_mulk_i32 s12, 0x147b
	s_lshr_b32 s12, s12, 17
	v_writelane_b32 v245, s12, 6
	s_mulk_i32 s12, 0x64
	s_sub_i32 s11, s11, s12
	s_and_b32 s11, s11, 0xffff
	v_writelane_b32 v245, s11, 7
	s_add_i32 s11, s3, 0xffffb200
	s_lshr_b32 s11, s11, 5
	v_writelane_b32 v245, s11, 9
	s_add_i32 s11, s3, 0xde00
	s_and_b32 s12, s11, 0xffff
	s_mul_i32 s12, s12, 0xba2f
	s_lshr_b32 s12, s12, 23
	v_writelane_b32 v245, s12, 10
	s_mulk_i32 s12, 0xb0
	s_sub_i32 s11, s11, s12
	s_and_b32 s11, s11, 0xffff
	s_add_i32 s5, s3, 0xbb00
	v_writelane_b32 v245, s11, 12
	s_add_i32 s11, s3, 0xffffe600
	s_bfe_u32 s6, s5, 0x6000a
	s_lshr_b32 s11, s11, 5
	v_bfe_u32 v141, v2, 3, 5
	v_and_b32_e32 v3, 7, v2
	v_min_u32_sdwa v4, v2, s4 dst_sel:DWORD dst_unused:UNUSED_PAD src0_sel:BYTE_0 src1_sel:DWORD
	v_mul_u32_u24_e32 v7, 0x540, v131
	v_lshlrev_b32_e32 v6, 4, v6
	s_mulk_i32 s6, 0x2493
	v_writelane_b32 v245, s11, 13
	s_mul_hi_i32 s11, s3, 0x4ec4ec4f
	v_lshrrev_b32_e32 v161, 2, v4
	v_and_b32_e32 v5, 3, v4
	v_lshlrev_b32_e32 v134, 3, v3
	v_add3_u32 v175, 0, v7, v6
	v_mul_u32_u24_e32 v6, 0x540, v141
	v_mul_u32_u24_e32 v3, 0xa0, v3
	s_lshr_b32 s6, s6, 16
	s_lshr_b32 s12, s11, 31
	s_ashr_i32 s11, s11, 5
	v_add3_u32 v177, 0, v6, v3
	v_mul_u32_u24_e32 v3, 0x540, v161
	v_lshlrev_b32_e32 v132, 4, v5
	s_mul_i32 s7, s6, 0x1c00
	s_add_i32 s11, s11, s12
	v_add3_u32 v178, 0, v3, v132
	s_sub_i32 s5, s5, s7
	v_writelane_b32 v248, s11, 49
	s_mulk_i32 s11, 0x68
	v_lshlrev_b32_e32 v3, 2, v2
	s_and_b32 s7, s5, 31
	s_bfe_u32 s5, s5, 0xb0005
	s_and_b32 s8, s8, 0xffff
	s_sub_i32 s3, s3, s11
	v_and_b32_e32 v136, 60, v3
	v_lshrrev_b32_e32 v3, 1, v2
	v_bfe_u32 v2, v2, 4, 2
	v_writelane_b32 v248, s3, 51
	v_lshl_or_b32 v138, s2, 2, v2
	v_writelane_b32 v245, s14, 15
	s_and_b64 s[2:3], s[14:15], exec
	s_cselect_b32 s2, s6, s9
	v_writelane_b32 v245, s15, 16
	v_writelane_b32 v245, s2, 17
	s_movk_i32 s4, 0x50
	v_mad_u32_u24 v197, v137, s4, 0
	v_writelane_b32 v245, s3, 18
	s_cselect_b32 s2, s5, s10
	v_writelane_b32 v245, s2, 19
	s_cselect_b32 s2, s7, s8
	v_writelane_b32 v245, s2, 20
	s_movk_i32 s2, 0x800
	s_cselect_b32 s4, 0x1c00, s2
	v_writelane_b32 v245, s4, 21
	v_readlane_b32 s56, v246, 16
	v_lshlrev_b32_e32 v130, 2, v137
	v_mov_b32_e32 v133, 0
	v_lshlrev_b32_e32 v4, 2, v5
	v_lshl_add_u32 v198, v138, 2, 0
	v_lshlrev_b32_e32 v140, 3, v2
	v_writelane_b32 v245, s5, 22
	s_cselect_b32 s2, s2, 0x1c00
	v_readlane_b32 s64, v246, 24
	v_readlane_b32 s65, v246, 25
	v_readlane_b32 s68, v246, 28
	v_or_b32_e32 v135, 16, v131
	v_xor_b32_e32 v167, 0xff, v131
	v_xor_b32_e32 v169, 0xef, v131
	v_xor_b32_e32 v171, 0xff, v141
	v_xor_b32_e32 v173, 0xff, v161
	s_mov_b32 s73, 0
	v_add_u32_e32 v176, 0x5400, v175
	v_xor_b32_e32 v179, 0xdf, v131
	v_or_b32_e32 v180, 32, v131
	v_xor_b32_e32 v181, 0xcf, v131
	v_or_b32_e32 v182, 48, v131
	v_xor_b32_e32 v183, 0xdf, v141
	v_or_b32_e32 v184, 32, v141
	v_xor_b32_e32 v185, 0xdf, v161
	v_or_b32_e32 v186, 32, v161
	v_xor_b32_e32 v187, 0xbf, v131
	v_or_b32_e32 v189, 64, v131
	v_xor_b32_e32 v190, 0xaf, v131
	v_or_b32_e32 v191, 0x50, v131
	v_xor_b32_e32 v192, 0xbf, v141
	v_or_b32_e32 v193, 64, v141
	v_xor_b32_e32 v194, 0xbf, v161
	v_or_b32_e32 v195, 64, v161
	v_and_b32_e32 v196, 24, v3
	v_ashrrev_i32_e32 v139, 31, v138
	v_or_b32_e32 v199, 1, v140
	v_add_u32_e32 v200, 0xa800, v197
	v_add_u32_e32 v201, 0xad00, v198
	v_writelane_b32 v245, s2, 23
	s_cselect_b32 s2, 9, 7
	v_cmp_eq_u32_e64 s[4:5], 0, v137
	v_cmp_eq_u32_e64 s[6:7], 1, v137
	v_cmp_eq_u32_e64 s[8:9], 2, v137
	v_cmp_eq_u32_e64 s[10:11], 3, v137
	v_cmp_eq_u32_e64 s[12:13], 4, v137
	v_cmp_eq_u32_e64 s[14:15], 5, v137
	v_cmp_eq_u32_e64 s[16:17], 6, v137
	v_cmp_eq_u32_e64 s[18:19], 7, v137
	v_cmp_eq_u32_e64 s[20:21], 8, v137
	v_cmp_eq_u32_e64 s[22:23], 9, v137
	v_cmp_eq_u32_e64 s[24:25], 10, v137
	v_cmp_eq_u32_e64 s[26:27], 11, v137
	v_cmp_eq_u32_e64 s[28:29], 12, v137
	v_cmp_eq_u32_e64 s[30:31], 13, v137
	v_cmp_eq_u32_e64 s[34:35], 14, v137
	v_cmp_eq_u32_e64 s[36:37], 15, v137
	v_lshl_add_u64 v[142:143], s[64:65], 0, v[132:133]
	v_lshlrev_b32_e32 v144, 2, v4
	v_lshlrev_b32_e32 v146, 2, v130
	v_not_b32_e32 v202, 16
	s_mov_b32 s68, s90
	v_writelane_b32 v245, s2, 24
	v_readlane_b32 s57, v246, 17
	v_readlane_b32 s58, v246, 18
	v_readlane_b32 s59, v246, 19
	v_readlane_b32 s60, v246, 20
	v_readlane_b32 s61, v246, 21
	v_readlane_b32 s62, v246, 22
	v_readlane_b32 s63, v246, 23
	v_readlane_b32 s66, v246, 26
	v_readlane_b32 s67, v246, 27
	v_readlane_b32 s69, v246, 29
	v_readlane_b32 s70, v246, 30
	v_readlane_b32 s71, v246, 31
	s_branch .LBB0_609

; __device__ __forceinline__ int ptid() { int t = threadIdx.x; asm volatile("" : "+v"(t)); return t; }
; __device__ __forceinline__ void ph_naattn(const Params& p, float* lds, int wg, int nwg) {
;     const int tid = ptid(), wave = __builtin_amdgcn_readfirstlane(tid >> 6), lane = tid & 63, r = lane & 31, hh = lane >> 5;
;     float* tab = lds + wave * 512;
;     for (int u = wg * 8 + wave; u < 4096 + 256; u += nwg * 8) {
;         int b, h, qrow0, nband = 0, gr = 0, r0 = 0, q0 = 0;
;         if (u < 4096) { h = u & 15; int x = u >> 4; q0 = (x & 1) * 32; x >>= 1; gr = x & 63; b = x >> 6; qrow0 = b * TL + gr * 64 + q0; r0 = gr - 4; r0 = r0 < 0 ? 0 : (r0 > 56 ? 56 : r0); nband = 8; }
;         else { int x = u - 4096; h = x & 15; x >>= 4; b = x >> 3; qrow0 = NL + b * TC + (x & 7) * 32; }
;         if (nband) for (int i = lane; i < 465; i += 64) tab[i] = p.in[22][h * 465 + i];
;         pg8::bf16x8 qf[4];
; #pragma unroll
;         for (int ks = 0; ks < 4; ++ks) qf[ks] = *(const pg8::bf16x8*)(p.Qb + (size_t)(qrow0 + r) * 1024 + h * 64 + 16 * ks + 8 * hh);
;         const float mq = p.QM[(qrow0 + r) * 16 + h];
.LBB0_751:
	s_waitcnt vmcnt(0)
	v_mov_b32_e32 v2, v0
	v_readlane_b32 s2, v248, 25
	v_readfirstlane_b32 s0, v2
	s_ashr_i32 s1, s0, 6
	s_add_i32 s2, s1, s2
	s_cmpk_gt_i32 s2, 0x10ff
	v_readlane_b32 s3, v248, 26
	s_cselect_b32 s98, 1, 0
	v_readlane_b32 s99, v249, 61
	s_nop 3
	s_or_b32 s98, s98, s99
	s_cbranch_scc1 .LBB0_768
	v_and_b32_e32 v84, 31, v2
	v_bfe_u32 v3, v2, 5, 1
	v_lshlrev_b32_e32 v5, 4, v84
	v_readlane_b32 s8, v248, 5
	v_and_b32_e32 v69, 63, v2
	v_mov_b32_e32 v67, 0
	v_lshl_or_b32 v66, v3, 9, v5
	v_readlane_b32 s9, v248, 6
	v_lshlrev_b32_e32 v2, 4, v2
	s_lshl_b32 s1, s1, 11
	v_readlane_b32 s10, v248, 7
	v_readlane_b32 s11, v248, 8
	v_lshl_add_u64 v[70:71], s[8:9], 0, v[66:67]
	v_and_b32_e32 v66, 0x3f0, v2
	s_add_i32 s3, s1, 0
	s_lshr_b32 s4, s0, 6
	v_lshlrev_b32_e32 v4, 3, v3
	v_lshlrev_b32_e32 v68, 2, v3
	v_lshl_add_u64 v[72:73], s[10:11], 0, v[66:67]
	v_or_b32_e32 v2, 0x180, v69
	s_movk_i32 s0, 0x191
	v_lshlrev_b32_e32 v66, 4, v69
	v_readlane_b32 s8, v248, 25
	s_mov_b32 s7, 0
	v_lshl_add_u32 v85, v69, 2, s3
	v_cmp_gt_u32_e64 s[0:1], s0, v2
	v_lshl_add_u64 v[74:75], s[10:11], 0, v[66:67]
	s_add_i32 s10, s8, s4
	v_lshlrev_b32_e32 v76, 1, v4
	v_mov_b32_e32 v77, v67
	s_mov_b32 s11, 0x3fb8aa3b
	v_lshlrev_b32_e32 v66, 1, v68
	v_readlane_b32 s9, v248, 26

; #define RUN(grp, ...) do { for (int rep_ = 0; rep_ < ((PROBE == (grp)) ? 2 : 1); ++rep_) { __VA_ARGS__ } } while (0)
; __global__ void __launch_bounds__(NTHR, 2) k_all(Params p) {
;     ...
;     RUN(3, ph_rwscan(p, lds, wg, nwg, ct_split); ph_naattn(p, lds, wg, nwg);); xcd_barrier(bar);
.LBB0_768:
	v_readlane_b32 s98, v249, 62
	s_nop 3
	s_cmp_eq_u32 s98, 0
	s_cbranch_scc1 .Lswap_done
	s_mov_b32 s98, 0
	v_writelane_b32 v249, s98, 60
	v_writelane_b32 v249, s98, 62
	s_mov_b32 s98, 1
	v_writelane_b32 v249, s98, 61
	v_readlane_b32 s6, v249, 0
	v_readlane_b32 s12, v249, 1
	v_readlane_b32 s14, v249, 2
	v_readlane_b32 s15, v249, 3
	v_readlane_b32 s18, v249, 4
	v_readlane_b32 s19, v249, 5
	v_readlane_b32 s20, v249, 6
	v_readlane_b32 s21, v249, 7
	v_readlane_b32 s22, v249, 8
	v_readlane_b32 s23, v249, 9
	v_readlane_b32 s24, v249, 10
	v_readlane_b32 s25, v249, 11
	v_readlane_b32 s34, v249, 12
	v_readlane_b32 s35, v249, 13
	v_readlane_b32 s39, v249, 14
	v_readlane_b32 s46, v249, 15
	v_readlane_b32 s47, v249, 16
	v_readlane_b32 s48, v249, 17
	v_readlane_b32 s49, v249, 18
	v_readlane_b32 s74, v249, 19
	v_readlane_b32 s75, v249, 20
	v_readlane_b32 s76, v249, 21
	v_readlane_b32 s77, v249, 22
	v_readlane_b32 s88, v249, 23
	v_readlane_b32 s90, v249, 24
	v_readlane_b32 s91, v249, 25
	v_readlane_b32 s92, v249, 26
	v_readlane_b32 s93, v249, 27
	v_readlane_b32 s96, v249, 28
	v_readlane_b32 s97, v249, 29
	v_mov_b32_e32 v5, v250
	v_mov_b32_e32 v245, v251
	v_mov_b32_e32 v248, v252
	s_nop 4
	s_branch .Lswap_top

; __global__ void __launch_bounds__(NTHR, 2) k_all(Params p) {
	.amdhsa_kernel _Z5k_all6Params
		.amdhsa_group_segment_fixed_size 0
		.amdhsa_private_segment_fixed_size 0
		.amdhsa_kernarg_size 1032
		.amdhsa_user_sgpr_count 2
		.amdhsa_user_sgpr_dispatch_ptr 0
		.amdhsa_user_sgpr_queue_ptr 0
		.amdhsa_user_sgpr_kernarg_segment_ptr 1
		.amdhsa_user_sgpr_dispatch_id 0
		.amdhsa_user_sgpr_kernarg_preload_length 0
		.amdhsa_user_sgpr_kernarg_preload_offset 0
		.amdhsa_user_sgpr_private_segment_size 0
		.amdhsa_uses_dynamic_stack 0
		.amdhsa_enable_private_segment 0
		.amdhsa_system_sgpr_workgroup_id_x 1
		.amdhsa_system_sgpr_workgroup_id_y 0
		.amdhsa_system_sgpr_workgroup_id_z 0
		.amdhsa_system_sgpr_workgroup_info 0
		.amdhsa_system_vgpr_workitem_id 0
		.amdhsa_next_free_vgpr 256
		.amdhsa_next_free_sgpr 102
		.amdhsa_accum_offset 256
		.amdhsa_reserve_vcc 1
		.amdhsa_float_round_mode_32 0
		.amdhsa_float_round_mode_16_64 0
		.amdhsa_float_denorm_mode_32 3
		.amdhsa_float_denorm_mode_16_64 3
		.amdhsa_dx10_clamp 1
		.amdhsa_ieee_mode 1
		.amdhsa_fp16_overflow 0
		.amdhsa_tg_split 0
		.amdhsa_exception_fp_ieee_invalid_op 0
		.amdhsa_exception_fp_denorm_src 0
		.amdhsa_exception_fp_ieee_div_zero 0
		.amdhsa_exception_fp_ieee_overflow 0
		.amdhsa_exception_fp_ieee_underflow 0
		.amdhsa_exception_fp_ieee_inexact 0
		.amdhsa_exception_int_div_zero 0
	.end_amdhsa_kernel

; __global__ void __launch_bounds__(NTHR, 2) k_all(Params p) {
amdhsa.kernels:
  - .agpr_count:     0
    .args:
      - .offset:         0
        .size:           776
        .value_kind:     by_value
      - .offset:         776
        .size:           4
        .value_kind:     hidden_block_count_x
      - .offset:         780
        .size:           4
        .value_kind:     hidden_block_count_y
      - .offset:         784
        .size:           4
        .value_kind:     hidden_block_count_z
      - .offset:         788
        .size:           2
        .value_kind:     hidden_group_size_x
      - .offset:         790
        .size:           2
        .value_kind:     hidden_group_size_y
      - .offset:         792
        .size:           2
        .value_kind:     hidden_group_size_z
      - .offset:         794
        .size:           2
        .value_kind:     hidden_remainder_x
      - .offset:         796
        .size:           2
        .value_kind:     hidden_remainder_y
      - .offset:         798
        .size:           2
        .value_kind:     hidden_remainder_z
      - .offset:         816
        .size:           8
        .value_kind:     hidden_global_offset_x
      - .offset:         824
        .size:           8
        .value_kind:     hidden_global_offset_y
      - .offset:         832
        .size:           8
        .value_kind:     hidden_global_offset_z
      - .offset:         840
        .size:           2
        .value_kind:     hidden_grid_dims
      - .offset:         896
        .size:           4
        .value_kind:     hidden_dynamic_lds_size
    .group_segment_fixed_size: 0
    .kernarg_segment_align: 8
    .kernarg_segment_size: 1032
    .language:       OpenCL C
    .language_version:
      - 2
      - 0
    .max_flat_workgroup_size: 512
    .name:           _Z5k_all6Params
    .private_segment_fixed_size: 0
    .sgpr_count:     108
    .sgpr_spill_count: 270
    .symbol:         _Z5k_all6Params.kd
    .uniform_work_group_size: 1
    .uses_dynamic_stack: false
    .vgpr_count:     256
    .vgpr_spill_count: 0
    .wavefront_size: 64
